# P2 states: chunk-state tile staged in LDS and written one head later as 2 row-contiguous dwordx4 stores per wave instead of 4 scattered dwordx2 stores
# speedup vs baseline: 1.0052x; 1.0052x over previous
.LBB0_397:
	v_and_b32_e32 v216, 15, v0
	v_bfe_u32 v217, v0, 4, 2
	v_lshrrev_b32_e32 v218, 6, v0
	v_mul_u32_u24_e32 v212, 0x110, v216
	v_lshl_add_u32 v212, v218, 5, v212
	v_lshl_add_u32 v212, v217, 3, v212
	v_add_u32_e32 v212, 0x13000, v212
	v_lshl_add_u32 v213, v218, 3, v217
	v_mul_u32_u24_e32 v213, 0x110, v213
	v_lshl_add_u32 v213, v216, 4, v213
	v_add_u32_e32 v213, 0x13000, v213
	v_mul_u32_u24_e32 v214, 0x7e0, v218
	v_mul_u32_u24_e32 v219, 0xf8, v217
	v_add_u32_e32 v214, v214, v219
	v_mul_u32_u24_e32 v219, 0xf0, v216
	v_sub_u32_e32 v214, v214, v219
	v_add_u32_e32 v214, 0x1000, v214
	v_mov_b32_e32 v215, 0
	s_bfe_u32 s56, s55, 0x60003
	s_lshl_b32 s42, s56, 7
	s_and_b32 s39, s55, 7
	s_ashr_i32 s40, s55, 9
	v_or_b32_e32 v2, s42, v23
	s_lshl_b32 s41, s40, 13
	v_lshl_or_b32 v6, s39, 9, v1
	v_cmp_eq_u32_e64 s[12:13], 0, v2
	s_or_b32 s38, s42, s41
	v_lshlrev_b32_e32 v20, 1, v6
	v_cndmask_b32_e64 v42, v58, 0, s[12:13]
	v_lshl_add_u64 v[2:3], s[2:3], 0, v[20:21]
	v_add_u32_e32 v4, s38, v42
	v_mad_i64_i32 v[4:5], s[58:59], v4, s45, v[2:3]
	v_cndmask_b32_e64 v40, v59, 0, s[12:13]
	global_load_dword v49, v[4:5], off
	v_add_u32_e32 v4, s38, v40
	v_mad_i64_i32 v[4:5], s[58:59], v4, s45, v[2:3]
	v_cndmask_b32_e64 v38, v60, 0, s[12:13]
	global_load_dword v50, v[4:5], off
	v_add_u32_e32 v4, s38, v38
	v_mad_i64_i32 v[4:5], s[58:59], v4, s45, v[2:3]
	global_load_dword v51, v[4:5], off
	v_or_b32_e32 v4, s38, v23
	v_mad_i64_i32 v[4:5], s[58:59], v4, s45, v[2:3]
	global_load_dword v45, v[4:5], off
	v_or_b32_e32 v4, s38, v61
	v_mad_i64_i32 v[4:5], s[58:59], v4, s45, v[2:3]
	global_load_dword v46, v[4:5], off
	v_or_b32_e32 v4, s38, v62
	v_mad_i64_i32 v[4:5], s[58:59], v4, s45, v[2:3]
	global_load_dword v48, v[4:5], off
	v_or_b32_e32 v4, s38, v63
	v_mad_i64_i32 v[4:5], s[58:59], v4, s45, v[2:3]
	global_load_dword v44, v[4:5], off
	v_or_b32_e32 v4, s38, v64
	v_mad_i64_i32 v[4:5], s[58:59], v4, s45, v[2:3]
	global_load_dword v47, v[4:5], off
	v_or_b32_e32 v4, s38, v65
	v_mad_i64_i32 v[4:5], s[58:59], v4, s45, v[2:3]
	global_load_dword v41, v[4:5], off
	v_or_b32_e32 v4, s38, v66
	v_mad_i64_i32 v[4:5], s[58:59], v4, s45, v[2:3]
	v_readlane_b32 s60, v253, 18
	global_load_dword v43, v[4:5], off
	v_or_b32_e32 v4, s38, v67
	v_readlane_b32 s74, v253, 32
	v_readlane_b32 s75, v253, 33
	v_mad_i64_i32 v[2:3], s[58:59], v4, s45, v[2:3]
	v_readlane_b32 s68, v253, 26
	v_readlane_b32 s69, v253, 27
	v_readlane_b32 s70, v253, 28
	v_readlane_b32 s71, v253, 29
	v_readlane_b32 s72, v253, 30
	v_readlane_b32 s73, v253, 31
	s_mov_b32 s26, s84
	s_mov_b64 s[90:91], s[74:75]
	global_load_dword v39, v[2:3], off
	v_lshlrev_b32_e32 v2, 2, v6
	s_mov_b64 s[86:87], s[70:71]
	s_mov_b64 s[88:89], s[72:73]
	global_load_dwordx2 v[12:13], v2, s[86:87]
	global_load_dwordx2 v[16:17], v2, s[18:19]
	global_load_dwordx2 v[10:11], v2, s[20:21]
	global_load_dwordx2 v[18:19], v2, s[22:23]
	global_load_dwordx2 v[14:15], v2, s[88:89]
	v_or_b32_e32 v2, s38, v248
	v_ashrrev_i32_e32 v3, 31, v2
	v_lshlrev_b64 v[4:5], 8, v[2:3]
	v_or_b32_e32 v2, 64, v2
	s_mov_b64 s[84:85], s[68:69]
	s_lshl_b32 s57, s39, 3
	v_ashrrev_i32_e32 v3, 31, v2
	s_mov_b32 s84, s26
	s_add_i32 s26, s57, s26
	v_lshlrev_b64 v[2:3], 8, v[2:3]
	v_readlane_b32 s61, v253, 19
	v_readlane_b32 s62, v253, 20
	v_readlane_b32 s63, v253, 21
	v_readlane_b32 s64, v253, 22
	v_readlane_b32 s65, v253, 23
	v_readlane_b32 s66, v253, 24
	v_readlane_b32 s67, v253, 25
	v_lshl_add_u64 v[4:5], s[24:25], 0, v[4:5]
	s_lshl_b32 s26, s26, 2
	v_lshl_add_u64 v[2:3], s[24:25], 0, v[2:3]
	v_lshl_add_u64 v[4:5], v[4:5], 0, s[26:27]
	v_lshl_add_u64 v[2:3], v[2:3], 0, s[26:27]
	v_readlane_b32 s60, v253, 34
	v_lshl_or_b32 v6, s39, 7, v68
	v_cmp_gt_i32_e32 vcc, s42, v102
	global_load_dword v29, v[4:5], off
	global_load_dword v32, v[2:3], off
	v_mov_b32_e32 v2, s26
	v_readlane_b32 s61, v253, 35
	v_lshlrev_b32_e32 v20, 1, v6
	v_cndmask_b32_e32 v4, 0, v70, vcc
	global_load_dword v33, v2, s[90:91]
	v_add_u32_e32 v4, s38, v4
	v_or_b32_e32 v7, s38, v69
	global_load_dword v34, v2, s[60:61]
	v_lshl_add_u64 v[2:3], s[2:3], 0, v[20:21]
	v_mad_i64_i32 v[4:5], s[58:59], v4, s45, v[2:3]
	global_load_dword v20, v[4:5], off
	v_cndmask_b32_e32 v4, 0, v71, vcc
	v_add_u32_e32 v4, s38, v4
	v_mad_i64_i32 v[4:5], s[58:59], v4, s45, v[2:3]
	global_load_dword v30, v[4:5], off
	v_cndmask_b32_e32 v4, 0, v72, vcc
	v_add_u32_e32 v4, s38, v4
	v_mad_i64_i32 v[4:5], s[58:59], v4, s45, v[2:3]
	global_load_dword v31, v[4:5], off
	v_mad_i64_i32 v[4:5], s[58:59], v7, s45, v[2:3]
	global_load_dword v122, v[4:5], off
	v_or_b32_e32 v4, 1, v7
	v_mad_i64_i32 v[4:5], s[58:59], v4, s45, v[2:3]
	global_load_dword v123, v[4:5], off
	v_or_b32_e32 v4, 2, v7
	v_mad_i64_i32 v[4:5], s[58:59], v4, s45, v[2:3]
	global_load_dword v124, v[4:5], off
	v_or_b32_e32 v4, 3, v7
	v_mad_i64_i32 v[4:5], s[58:59], v4, s45, v[2:3]
	global_load_dword v120, v[4:5], off
	v_or_b32_e32 v4, 4, v7
	v_mad_i64_i32 v[4:5], s[58:59], v4, s45, v[2:3]
	global_load_dword v121, v[4:5], off
	v_or_b32_e32 v4, 5, v7
	v_mad_i64_i32 v[4:5], s[58:59], v4, s45, v[2:3]
	global_load_dword v118, v[4:5], off
	v_or_b32_e32 v4, 6, v7
	v_mad_i64_i32 v[4:5], s[58:59], v4, s45, v[2:3]
	global_load_dword v119, v[4:5], off
	v_or_b32_e32 v4, s38, v103
	v_mad_i64_i32 v[4:5], s[58:59], v4, s45, v[2:3]
	global_load_dword v117, v[4:5], off
	v_or_b32_e32 v4, s38, v74
	v_mad_i64_i32 v[4:5], s[58:59], v4, s45, v[2:3]
	global_load_dword v113, v[4:5], off
	v_or_b32_e32 v4, s38, v75
	v_mad_i64_i32 v[4:5], s[58:59], v4, s45, v[2:3]
	global_load_dword v116, v[4:5], off
	v_or_b32_e32 v4, s38, v76
	v_mad_i64_i32 v[4:5], s[58:59], v4, s45, v[2:3]
	global_load_dword v114, v[4:5], off
	v_or_b32_e32 v4, s38, v73
	v_mad_i64_i32 v[4:5], s[58:59], v4, s45, v[2:3]
	global_load_dword v57, v[4:5], off
	v_or_b32_e32 v4, s38, v77
	v_mad_i64_i32 v[4:5], s[58:59], v4, s45, v[2:3]
	global_load_dword v112, v[4:5], off
	v_or_b32_e32 v4, s38, v78
	v_mad_i64_i32 v[4:5], s[58:59], v4, s45, v[2:3]
	global_load_dword v115, v[4:5], off
	v_or_b32_e32 v4, s38, v79
	v_mad_i64_i32 v[4:5], s[58:59], v4, s45, v[2:3]
	global_load_dword v55, v[4:5], off
	v_or_b32_e32 v4, s38, v80
	v_mad_i64_i32 v[4:5], s[58:59], v4, s45, v[2:3]
	global_load_dword v56, v[4:5], off
	v_or_b32_e32 v4, s38, v81
	v_mad_i64_i32 v[4:5], s[58:59], v4, s45, v[2:3]
	global_load_dword v53, v[4:5], off
	v_or_b32_e32 v4, s38, v82
	v_mad_i64_i32 v[4:5], s[58:59], v4, s45, v[2:3]
	global_load_dword v54, v[4:5], off
	v_or_b32_e32 v4, s38, v83
	v_mad_i64_i32 v[2:3], s[38:39], v4, s45, v[2:3]
	v_lshlrev_b32_e32 v6, 2, v6
	global_load_dword v52, v[2:3], off
	global_load_dwordx2 v[4:5], v6, s[86:87]
	global_load_dwordx2 v[8:9], v6, s[18:19]
	s_nop 0
	global_load_dwordx2 v[2:3], v6, s[20:21]
	global_load_dwordx2 v[36:37], v6, s[22:23]
	s_nop 0
	global_load_dwordx2 v[6:7], v6, s[88:89]
	s_waitcnt vmcnt(28)
	v_add_f32_e32 v29, v29, v33
	v_cmp_nlt_f32_e32 vcc, s46, v29
	v_readlane_b32 s62, v253, 36
	v_readlane_b32 s63, v253, 37
	v_readlane_b32 s64, v253, 38
	v_readlane_b32 s65, v253, 39
	v_readlane_b32 s66, v253, 40
	v_readlane_b32 s67, v253, 41
	v_readlane_b32 s68, v253, 42
	v_readlane_b32 s69, v253, 43
	v_readlane_b32 s70, v253, 44
	v_readlane_b32 s71, v253, 45
	v_readlane_b32 s72, v253, 46
	v_readlane_b32 s73, v253, 47
	v_readlane_b32 s74, v253, 48
	v_readlane_b32 s75, v253, 49
	s_barrier
	s_and_saveexec_b64 s[38:39], vcc
	s_cbranch_execz .LBB0_399
	v_mul_f32_e32 v29, 0x3fb8aa3b, v29
	v_exp_f32_e32 v35, v29
	s_nop 0
	v_add_f32_e32 v29, 1.0, v35
	v_frexp_mant_f32_e32 v128, v29
	v_cvt_f64_f32_e32 v[126:127], v29
	v_add_f32_e32 v125, -1.0, v29
	v_frexp_exp_i32_f64_e32 v126, v[126:127]
	v_cmp_gt_f32_e32 vcc, s47, v128
	v_sub_f32_e32 v129, v125, v29
	v_sub_f32_e32 v125, v35, v125
	v_subbrev_co_u32_e32 v134, vcc, 0, v126, vcc
	v_add_f32_e32 v129, 1.0, v129
	v_sub_u32_e32 v126, 0, v134
	v_add_f32_e32 v125, v125, v129
	v_ldexp_f32 v29, v29, v126
	v_ldexp_f32 v125, v125, v126
	v_add_f32_e32 v126, -1.0, v29
	v_add_f32_e32 v127, 1.0, v126
	v_sub_f32_e32 v127, v29, v127
	v_add_f32_e32 v128, v125, v127
	v_add_f32_e32 v127, 1.0, v29
	v_add_f32_e32 v129, -1.0, v127
	v_sub_f32_e32 v29, v29, v129
	v_add_f32_e32 v29, v125, v29
	v_add_f32_e32 v125, v127, v29
	v_rcp_f32_e32 v135, v125
	v_sub_f32_e32 v127, v125, v127
	v_sub_f32_e32 v29, v29, v127
	v_add_f32_e32 v127, v126, v128
	v_sub_f32_e32 v126, v127, v126
	v_mul_f32_e32 v137, v127, v135
	v_sub_f32_e32 v136, v128, v126
	v_mul_f32_e32 v128, v125, v137
	v_fma_f32 v130, v137, v125, -v128
	v_fmac_f32_e32 v130, v137, v29
	v_add_f32_e32 v126, v128, v130
	v_sub_f32_e32 v129, v127, v126
	v_pk_add_f32 v[132:133], v[126:127], v[128:129] neg_lo:[0,1] neg_hi:[0,1]
	v_mov_b32_e32 v131, v126
	v_pk_add_f32 v[126:127], v[132:133], v[130:131] neg_lo:[0,1] neg_hi:[0,1]
	v_cmp_neq_f32_e32 vcc, s50, v35
	v_add_f32_e32 v127, v136, v127
	v_add_f32_e32 v126, v126, v127
	v_add_f32_e32 v127, v129, v126
	v_mul_f32_e32 v136, v135, v127
	v_mul_f32_e32 v128, v125, v136
	v_fma_f32 v130, v136, v125, -v128
	v_fmac_f32_e32 v130, v136, v29
	v_sub_f32_e32 v29, v129, v127
	v_add_f32_e32 v29, v126, v29
	v_add_f32_e32 v126, v128, v130
	v_sub_f32_e32 v129, v127, v126
	v_pk_add_f32 v[132:133], v[126:127], v[128:129] neg_lo:[0,1] neg_hi:[0,1]
	v_mov_b32_e32 v131, v126
	v_pk_add_f32 v[126:127], v[132:133], v[130:131] neg_lo:[0,1] neg_hi:[0,1]
	v_add_f32_e32 v125, v137, v136
	v_add_f32_e32 v29, v29, v127
	v_add_f32_e32 v29, v126, v29
	v_add_f32_e32 v29, v129, v29
	v_sub_f32_e32 v126, v125, v137
	v_mul_f32_e32 v29, v135, v29
	v_sub_f32_e32 v126, v136, v126
	v_add_f32_e32 v127, v126, v29
	v_add_f32_e32 v128, v125, v127
	v_cvt_f32_i32_e32 v126, v134
	v_mul_f32_e32 v130, v128, v128
	v_fmamk_f32 v29, v130, 0x3e9b6dac, v105
	v_sub_f32_e32 v125, v128, v125
	v_fmaak_f32 v29, v130, v29, 0x3f2aaada
	v_sub_f32_e32 v125, v127, v125
	v_mul_f32_e32 v127, v128, v130
	v_pk_mul_f32 v[130:131], v[126:127], v[28:29]
	v_ldexp_f32 v129, v128, 1
	v_fma_f32 v128, v126, s49, -v130
	v_fmac_f32_e32 v128, 0xb102e308, v126
	v_pk_add_f32 v[126:127], v[130:131], v[128:129]
	v_ldexp_f32 v125, v125, 1
	v_sub_f32_e32 v29, v127, v129
	v_sub_f32_e32 v29, v131, v29
	v_add_f32_e32 v133, v125, v29
	v_mov_b32_e32 v132, v130
	v_pk_add_f32 v[130:131], v[126:127], v[130:131] neg_lo:[0,1] neg_hi:[0,1]
	v_pk_add_f32 v[134:135], v[126:127], v[132:133]
	v_mov_b32_e32 v129, v126
	v_mov_b32_e32 v131, v135
	v_pk_add_f32 v[136:137], v[128:129], v[130:131] neg_lo:[0,1] neg_hi:[0,1]
	v_pk_add_f32 v[128:129], v[128:129], v[130:131]
	v_mov_b32_e32 v132, v133
	v_pk_add_f32 v[130:131], v[128:129], v[126:127] op_sel:[1,0] op_sel_hi:[0,1] neg_lo:[0,1] neg_hi:[0,1]
	v_pk_add_f32 v[138:139], v[134:135], v[130:131] op_sel_hi:[1,0] neg_lo:[0,1] neg_hi:[0,1]
	v_mov_b32_e32 v134, v135
	v_mov_b32_e32 v135, v129
	v_pk_mov_b32 v[130:131], v[126:127], v[130:131] op_sel:[1,0]
	v_mov_b32_e32 v133, v126
	v_pk_add_f32 v[130:131], v[134:135], v[130:131] neg_lo:[0,1] neg_hi:[0,1]
	v_mov_b32_e32 v138, v136
	v_pk_add_f32 v[126:127], v[132:133], v[130:131] neg_lo:[0,1] neg_hi:[0,1]
	v_mov_b32_e32 v137, v129
	v_pk_add_f32 v[130:131], v[138:139], v[126:127]
	s_nop 0
	v_pk_add_f32 v[132:133], v[130:131], v[130:131] op_sel:[0,1] op_sel_hi:[1,0]
	s_nop 0
	v_pk_add_f32 v[128:129], v[128:129], v[132:133] op_sel:[1,0] op_sel_hi:[0,1]
	v_mov_b32_e32 v131, v128
	v_pk_add_f32 v[134:135], v[130:131], v[136:137] neg_lo:[0,1] neg_hi:[0,1]
	v_mov_b32_e32 v127, v132
	v_sub_f32_e32 v29, v130, v134
	v_pk_add_f32 v[126:127], v[126:127], v[134:135] neg_lo:[0,1] neg_hi:[0,1]
	v_sub_f32_e32 v29, v136, v29
	v_add_f32_e32 v29, v126, v29
	v_add_f32_e32 v29, v29, v127
	v_add_f32_e32 v29, v128, v29
	v_cndmask_b32_e32 v29, v109, v29, vcc
	v_cmp_ngt_f32_e32 vcc, -1.0, v35
	s_nop 1
	v_cndmask_b32_e32 v29, v110, v29, vcc
	v_cmp_neq_f32_e32 vcc, -1.0, v35
	s_nop 1
	v_cndmask_b32_e32 v29, v111, v29, vcc
	v_cmp_lt_f32_e64 vcc, |v35|, s51
	s_nop 1
	v_cndmask_b32_e32 v29, v29, v35, vcc

.LBB0_402:
	s_or_b64 exec, exec, s[42:43]
	s_cmp_eq_u32 s62, 0
	s_cbranch_scc1 .Lp2_w0
	s_waitcnt vmcnt(2)
	s_branch .Lp2_wd

.Lp2_wd:
	v_cndmask_b32_e64 v18, v168, 0, s[12:13]
	v_cndmask_b32_e64 v19, v169, 0, s[12:13]
	v_cndmask_b32_e64 v20, v170, 0, s[12:13]
	v_lshlrev_b32_e32 v120, 16, v18
	v_and_b32_e32 v131, 0xffff0000, v18
	v_lshlrev_b32_e32 v121, 16, v19
	v_and_b32_e32 v132, 0xffff0000, v19
	v_lshlrev_b32_e32 v122, 16, v20
	v_and_b32_e32 v133, 0xffff0000, v20
	v_lshlrev_b32_e32 v123, 16, v171
	v_and_b32_e32 v134, 0xffff0000, v171
	v_lshlrev_b32_e32 v124, 16, v172
	v_and_b32_e32 v135, 0xffff0000, v172
	v_lshlrev_b32_e32 v125, 16, v173
	v_and_b32_e32 v136, 0xffff0000, v173
	v_lshlrev_b32_e32 v126, 16, v174
	v_and_b32_e32 v137, 0xffff0000, v174
	v_lshlrev_b32_e32 v127, 16, v175
	v_and_b32_e32 v138, 0xffff0000, v175
	v_lshlrev_b32_e32 v128, 16, v176
	v_and_b32_e32 v139, 0xffff0000, v176
	v_lshlrev_b32_e32 v129, 16, v177
	v_and_b32_e32 v140, 0xffff0000, v177
	v_lshlrev_b32_e32 v130, 16, v178
	v_and_b32_e32 v141, 0xffff0000, v178
	v_mov_b64_e32 v[48:49], v[180:181]
	v_mov_b64_e32 v[56:57], v[182:183]
	v_mov_b64_e32 v[46:47], v[184:185]
	v_mov_b64_e32 v[54:55], v[186:187]
	v_mov_b64_e32 v[50:51], v[188:189]
	v_lshl_add_u64 v[34:35], v[34:35], 0, s[36:37]
	v_lshl_add_u64 v[36:37], v[36:37], 0, s[36:37]
	v_lshl_add_u64 v[38:39], v[38:39], 0, s[36:37]
	v_lshl_add_u64 v[40:41], v[40:41], 0, s[36:37]
	v_lshl_add_u64 v[42:43], v[42:43], 0, s[36:37]
	s_cmpk_eq_i32 s38, 0x600
	s_cbranch_scc1 .Lp2_pf_skip
	s_mov_b32 s76, 0x45c00000
	s_mov_b32 s77, 0
	s_movk_i32 s78, 0x3000
	s_mov_b32 s79, 0
	s_movk_i32 s80, 0x6000
	s_mov_b32 s81, 0
	v_lshl_add_u64 v[190:191], s[92:93], 0, v[42:43]
	v_lshl_add_u64 v[192:193], s[92:93], 0, v[40:41]
	v_lshl_add_u64 v[194:195], s[92:93], 0, v[38:39]
	v_lshl_add_u64 v[196:197], s[92:93], 0, v[36:37]
	global_load_dword v168, v[190:191], off
	global_load_dword v169, v[192:193], off
	global_load_dword v170, v[194:195], off
	v_lshl_add_u64 v[196:197], v[196:197], 0, s[76:77]
	global_load_dword v171, v[196:197], off offset:128
	v_lshl_add_u64 v[196:197], v[196:197], 0, s[78:79]
	global_load_dword v172, v[196:197], off offset:128
	v_lshl_add_u64 v[196:197], v[196:197], 0, s[78:79]
	global_load_dword v173, v[196:197], off offset:128
	v_lshl_add_u64 v[196:197], v[196:197], 0, s[78:79]
	global_load_dword v174, v[196:197], off offset:128
	v_lshl_add_u64 v[196:197], v[196:197], 0, s[78:79]
	global_load_dword v175, v[196:197], off offset:128
	v_lshl_add_u64 v[196:197], v[196:197], 0, s[78:79]
	global_load_dword v176, v[196:197], off offset:128
	v_lshl_add_u64 v[196:197], v[196:197], 0, s[78:79]
	global_load_dword v177, v[196:197], off offset:128
	v_lshl_add_u64 v[190:191], s[92:93], 0, v[34:35]
	global_load_dword v178, v[190:191], off
	v_lshl_add_u64 v[192:193], v[32:33], 0, s[38:39]
	global_load_dwordx2 v[180:181], v[192:193], off offset:512
	v_lshl_add_u64 v[192:193], v[192:193], 0, s[80:81]
	global_load_dwordx2 v[182:183], v[192:193], off offset:512
	v_lshl_add_u64 v[192:193], v[192:193], 0, s[80:81]
	global_load_dwordx2 v[184:185], v[192:193], off offset:512
	v_lshl_add_u64 v[192:193], v[192:193], 0, s[80:81]
	global_load_dwordx2 v[186:187], v[192:193], off offset:512
	v_lshl_add_u64 v[194:195], v[30:31], 0, s[38:39]
	global_load_dwordx2 v[188:189], v[194:195], off offset:256

.LBB0_403:
	s_cmp_eq_u32 s62, 0
	s_cbranch_scc1 .Lp2_nofl_a
	s_and_b32 s76, s62, 1
	s_xor_b32 s76, s76, 1
	s_mul_i32 s76, s76, 0x4400
	v_add_u32_e32 v216, s76, v213
	ds_read_b128 v[198:201], v216
	ds_read_b128 v[202:205], v216 offset:1088
	v_lshl_add_u64 v[206:207], s[92:93], 0, v[44:45]
	v_lshl_add_u64 v[206:207], v[206:207], 0, v[214:215]
	s_mov_b32 s76, 0x5dffb000
	s_mov_b32 s77, 0
	v_lshl_add_u64 v[206:207], v[206:207], 0, s[76:77]
.Lp2_nofl_a:
	s_bitcmp0_b32 s62, 0
	s_cselect_b64 s[40:41], -1, 0
	s_and_b64 s[42:43], s[40:41], exec
	s_cselect_b32 s42, s52, s53
	v_mov_b32_e32 v52, s26
	v_add3_u32 v53, s42, v92, v93
	ds_read_b32 v52, v52 offset:4604
	ds_read_b128 v[120:123], v53
	ds_read_b128 v[124:127], v53 offset:64
	ds_read_b128 v[128:131], v53 offset:4352
	ds_read_b128 v[132:135], v53 offset:4416
	ds_read_b128 v[136:139], v53 offset:8704
	ds_read_b128 v[140:143], v53 offset:8768
	ds_read_b128 v[144:147], v53 offset:13056
	ds_read_b128 v[148:151], v53 offset:13120
	s_waitcnt lgkmcnt(7)
	v_mfma_f32_16x16x32_bf16 v[120:123], v[14:17], v[120:123], 0
	s_waitcnt lgkmcnt(5)
	v_mfma_f32_16x16x32_bf16 v[128:131], v[14:17], v[128:131], 0
	s_waitcnt lgkmcnt(3)
	v_mfma_f32_16x16x32_bf16 v[136:139], v[14:17], v[136:139], 0
	s_waitcnt lgkmcnt(1)
	v_mfma_f32_16x16x32_bf16 v[144:147], v[14:17], v[144:147], 0
	s_cmp_eq_u32 s62, 0
	s_cbranch_scc1 .Lp2_nost_a
	global_store_dwordx4 v[206:207], v[198:201], off
	global_store_dwordx4 v[206:207], v[202:205], off offset:1024
.Lp2_nost_a:
	ds_read_b128 v[152:155], v53 offset:128
	ds_read_b128 v[156:159], v53 offset:4480
	ds_read_b128 v[160:163], v53 offset:8832
	ds_read_b128 v[164:167], v53 offset:13184
	v_mfma_f32_16x16x32_bf16 v[120:123], v[10:13], v[124:127], v[120:123]
	v_mfma_f32_16x16x32_bf16 v[124:127], v[10:13], v[132:135], v[128:131]
	v_mfma_f32_16x16x32_bf16 v[128:131], v[10:13], v[140:143], v[136:139]
	s_waitcnt lgkmcnt(4)
	v_mfma_f32_16x16x32_bf16 v[132:135], v[10:13], v[148:151], v[144:147]
	s_nop 0
	ds_read_b128 v[136:139], v53 offset:192
	ds_read_b128 v[140:143], v53 offset:4544
	ds_read_b128 v[144:147], v53 offset:8896
	ds_read_b128 v[148:151], v53 offset:13248
	s_waitcnt lgkmcnt(7)
	v_mfma_f32_16x16x32_bf16 v[120:123], v[6:9], v[152:155], v[120:123]
	s_waitcnt lgkmcnt(6)
	v_mfma_f32_16x16x32_bf16 v[124:127], v[6:9], v[156:159], v[124:127]
	s_waitcnt lgkmcnt(5)
	v_mfma_f32_16x16x32_bf16 v[128:131], v[6:9], v[160:163], v[128:131]
	s_waitcnt lgkmcnt(4)
	v_mfma_f32_16x16x32_bf16 v[132:135], v[6:9], v[164:167], v[132:135]
	s_waitcnt lgkmcnt(3)
	v_mfma_f32_16x16x32_bf16 v[120:123], v[2:5], v[136:139], v[120:123]
	s_waitcnt lgkmcnt(2)
	v_mfma_f32_16x16x32_bf16 v[124:127], v[2:5], v[140:143], v[124:127]
	s_waitcnt lgkmcnt(1)
	v_mfma_f32_16x16x32_bf16 v[128:131], v[2:5], v[144:147], v[128:131]
	s_waitcnt lgkmcnt(0)
	v_mfma_f32_16x16x32_bf16 v[132:135], v[2:5], v[148:151], v[132:135]
	s_nop 7
	s_nop 7
	v_cvt_pk_bf16_f32 v120, v120, v121
	v_cvt_pk_bf16_f32 v121, v122, v123
	v_cvt_pk_bf16_f32 v122, v124, v125
	v_cvt_pk_bf16_f32 v123, v126, v127
	v_cvt_pk_bf16_f32 v124, v128, v129
	v_cvt_pk_bf16_f32 v125, v130, v131
	v_cvt_pk_bf16_f32 v126, v132, v133
	v_cvt_pk_bf16_f32 v127, v134, v135
	s_and_b32 s76, s62, 1
	s_mul_i32 s76, s76, 0x4400
	v_add_u32_e32 v216, s76, v212
	ds_write_b64 v216, v[120:121]
	ds_write_b64 v216, v[122:123] offset:4352
	ds_write_b64 v216, v[124:125] offset:8704
	ds_write_b64 v216, v[126:127] offset:13056
	s_cmp_eq_u32 s84, s62
	s_cselect_b64 s[42:43], -1, 0
	s_and_b64 s[64:65], s[0:1], s[42:43]
	s_and_saveexec_b64 s[42:43], s[64:65]
	s_cbranch_execz .LBB0_402
	v_mul_f32_e32 v52, 0x3fb8aa3b, v52
	v_exp_f32_e32 v52, v52
	s_add_u32 s64, s92, s58
	s_addc_u32 s65, s93, s61
	global_store_dword v21, v52, s[64:65]
	s_branch .LBB0_402
.LBB0_405:
	s_and_b32 s76, s62, 1
	s_xor_b32 s76, s76, 1
	s_mul_i32 s76, s76, 0x4400
	v_add_u32_e32 v216, s76, v213
	ds_read_b128 v[198:201], v216
	ds_read_b128 v[202:205], v216 offset:1088
	v_lshl_add_u64 v[206:207], s[92:93], 0, v[44:45]
	v_lshl_add_u64 v[206:207], v[206:207], 0, v[214:215]
	s_mov_b32 s76, 0x5dffb000
	s_mov_b32 s77, 0
	v_lshl_add_u64 v[206:207], v[206:207], 0, s[76:77]
	v_add_u32_e32 v19, v94, v93
	ds_read_b32 v18, v21 offset:8188
	ds_read_b128 v[30:33], v19 offset:60416
	ds_read_b128 v[34:37], v19 offset:60480
	ds_read_b128 v[38:41], v19 offset:64768
	ds_read_b128 v[42:45], v19 offset:64832
	ds_read_b128 v[46:49], v107 offset:60416
	ds_read_b128 v[50:53], v107 offset:60480
	ds_read_b128 v[54:57], v108 offset:60416
	ds_read_b128 v[112:115], v108 offset:60480
	s_or_b32 s12, s60, s56
	s_ashr_i32 s13, s12, 31
	s_lshl_b64 s[12:13], s[12:13], 12
	v_mov_b32_e32 v129, s13
	v_or_b32_e32 v20, s12, v22
	s_waitcnt lgkmcnt(7)
	v_mfma_f32_16x16x32_bf16 v[30:33], v[14:17], v[30:33], 0
	s_waitcnt lgkmcnt(5)
	v_mfma_f32_16x16x32_bf16 v[38:41], v[14:17], v[38:41], 0
	s_waitcnt lgkmcnt(3)
	v_mfma_f32_16x16x32_bf16 v[46:49], v[14:17], v[46:49], 0
	s_waitcnt lgkmcnt(1)
	v_mfma_f32_16x16x32_bf16 v[14:17], v[14:17], v[54:57], 0
	global_store_dwordx4 v[206:207], v[198:201], off
	global_store_dwordx4 v[206:207], v[202:205], off offset:1024
	ds_read_b128 v[54:57], v19 offset:60544
	ds_read_b128 v[116:119], v19 offset:64896
	ds_read_b128 v[120:123], v107 offset:60544
	ds_read_b128 v[124:127], v108 offset:60544
	v_mfma_f32_16x16x32_bf16 v[30:33], v[10:13], v[34:37], v[30:33]
	v_mfma_f32_16x16x32_bf16 v[34:37], v[10:13], v[42:45], v[38:41]
	v_mfma_f32_16x16x32_bf16 v[38:41], v[10:13], v[50:53], v[46:49]
	s_waitcnt lgkmcnt(4)
	v_mfma_f32_16x16x32_bf16 v[10:13], v[10:13], v[112:115], v[14:17]
	s_nop 2
	ds_read_b128 v[14:17], v19 offset:60608
	ds_read_b128 v[42:45], v19 offset:64960
	ds_read_b128 v[46:49], v107 offset:60608
	ds_read_b128 v[50:53], v108 offset:60608
	s_waitcnt lgkmcnt(7)
	v_mfma_f32_16x16x32_bf16 v[30:33], v[6:9], v[54:57], v[30:33]
	s_waitcnt lgkmcnt(6)
	v_mfma_f32_16x16x32_bf16 v[34:37], v[6:9], v[116:119], v[34:37]
	s_waitcnt lgkmcnt(5)
	v_mfma_f32_16x16x32_bf16 v[38:41], v[6:9], v[120:123], v[38:41]
	s_waitcnt lgkmcnt(4)
	v_mfma_f32_16x16x32_bf16 v[6:9], v[6:9], v[124:127], v[10:13]
	s_waitcnt lgkmcnt(3)
	v_mfma_f32_16x16x32_bf16 v[10:13], v[2:5], v[14:17], v[30:33]
	s_waitcnt lgkmcnt(2)
	v_mfma_f32_16x16x32_bf16 v[14:17], v[2:5], v[42:45], v[34:37]
	s_waitcnt lgkmcnt(1)
	v_mfma_f32_16x16x32_bf16 v[30:33], v[2:5], v[46:49], v[38:41]
	s_waitcnt lgkmcnt(0)
	v_mfma_f32_16x16x32_bf16 v[2:5], v[2:5], v[50:53], v[6:9]
	s_or_b32 s26, s57, 7
	v_lshl_or_b32 v128, s26, 6, v20
	s_nop 0
	v_lshlrev_b64 v[8:9], 8, v[128:129]
	v_lshl_add_u64 v[8:9], v[24:25], 0, v[8:9]
	s_movk_i32 s12, 0x1000
	v_cvt_pk_bf16_f32 v6, v10, v11
	v_add_co_u32_e32 v10, vcc, s12, v8
	v_cvt_pk_bf16_f32 v7, v12, v13
	global_store_dwordx2 v[8:9], v[6:7], off
	s_nop 0
	v_addc_co_u32_e32 v11, vcc, 0, v9, vcc
	v_cvt_pk_bf16_f32 v6, v14, v15
	v_cvt_pk_bf16_f32 v7, v16, v17
	global_store_dwordx2 v[10:11], v[6:7], off
	v_add_co_u32_e32 v10, vcc, 0x2000, v8
	v_cvt_pk_bf16_f32 v6, v30, v31
	v_cvt_pk_bf16_f32 v7, v32, v33
	s_nop 1
	v_addc_co_u32_e32 v11, vcc, 0, v9, vcc
	global_store_dwordx2 v[10:11], v[6:7], off
	v_cvt_pk_bf16_f32 v2, v2, v3
	v_cvt_pk_bf16_f32 v3, v4, v5
	v_add_co_u32_e32 v4, vcc, 0x3000, v8
	s_nop 1
	v_addc_co_u32_e32 v5, vcc, 0, v9, vcc
	global_store_dwordx2 v[4:5], v[2:3], off
	s_and_saveexec_b64 s[12:13], s[28:29]
	s_cbranch_execz .LBB0_396
	s_lshl_b32 s38, s56, 6
	s_or_b32 s38, s38, s59
	s_or_b32 s38, s38, s26
	v_mul_f32_e32 v2, 0x3fb8aa3b, v18
	s_ashr_i32 s39, s38, 31
	v_exp_f32_e32 v2, v2
	s_lshl_b64 s[38:39], s[38:39], 2
	s_add_u32 s38, s33, s38
	s_addc_u32 s39, s44, s39
	global_store_dword v21, v2, s[38:39]
	s_branch .LBB0_396
